# v57 + 4-byte pad before the in-proj K-loop (MFMAs on 8-byte boundaries) with a compensating pad after it, downstream placement unchanged
# speedup vs baseline: 1.0002x; 1.0002x over previous
.LBB0_265:
	s_add_u32 s24, s6, 0xfff00080
	s_addc_u32 s25, s7, -1
	s_add_i32 s28, 0, 0x10000
	s_cmp_eq_u32 s58, 60
	s_cselect_b32 s27, s73, s25
	s_cselect_b32 s26, vcc_lo, s24
	s_cselect_b32 s25, s75, s13
	s_cselect_b32 s24, vcc_hi, s21
	s_add_i32 s71, 0, 0x14000
	v_add_u32_e32 v144, s28, v163
	v_add_u32_e32 v182, s71, v163
	s_waitcnt lgkmcnt(0)
	ds_read_b128 v[132:135], v144
	ds_read_b128 v[136:139], v144 offset:1024
	ds_read_b128 v[140:143], v144 offset:2048
	ds_read_b128 v[144:147], v144 offset:3072
	ds_read_b128 v[148:151], v182
	ds_read_b128 v[152:155], v182 offset:1024
	ds_read_b128 v[178:181], v182 offset:2048
	ds_read_b128 v[186:189], v182 offset:3072
	v_lshl_add_u64 v[182:183], s[6:7], 0, v[174:175]
	s_add_i32 m0, s46, 0xc000
	ds_read_b128 v[190:193], v184
	ds_read_b128 v[194:197], v184 offset:1024
	ds_read_b128 v[198:201], v184 offset:2048
	ds_read_b128 v[202:205], v184 offset:3072
	ds_read_b128 v[222:225], v184 offset:4096
	ds_read_b128 v[226:229], v184 offset:5120
	ds_read_b128 v[230:233], v184 offset:6144
	ds_read_b128 v[234:237], v184 offset:7168
	global_load_lds_dwordx4 v[182:183], off
	v_lshl_add_u64 v[182:183], s[6:7], 0, v[176:177]
	s_add_i32 m0, s46, 0xe000
	s_nop 0
	global_load_lds_dwordx4 v[182:183], off
	s_waitcnt vmcnt(8)
	s_waitcnt lgkmcnt(0)
	s_setprio 1
	s_barrier
	v_mfma_f32_16x16x32_bf16 v[120:123], v[132:135], v[190:193], v[120:123]
	v_mfma_f32_16x16x32_bf16 v[116:119], v[140:143], v[190:193], v[116:119]
	v_mfma_f32_16x16x32_bf16 v[104:107], v[132:135], v[198:201], v[104:107]
	v_mfma_f32_16x16x32_bf16 v[100:103], v[140:143], v[198:201], v[100:103]
	v_mfma_f32_16x16x32_bf16 v[88:91], v[132:135], v[222:225], v[88:91]
	v_mfma_f32_16x16x32_bf16 v[84:87], v[140:143], v[222:225], v[84:87]
	v_mfma_f32_16x16x32_bf16 v[72:75], v[132:135], v[230:233], v[72:75]
	v_mfma_f32_16x16x32_bf16 v[68:71], v[140:143], v[230:233], v[68:71]
	v_mfma_f32_16x16x32_bf16 v[120:123], v[136:139], v[194:197], v[120:123]
	v_mfma_f32_16x16x32_bf16 v[116:119], v[144:147], v[194:197], v[116:119]
	v_mfma_f32_16x16x32_bf16 v[104:107], v[136:139], v[202:205], v[104:107]
	v_mfma_f32_16x16x32_bf16 v[100:103], v[144:147], v[202:205], v[100:103]
	v_mfma_f32_16x16x32_bf16 v[88:91], v[136:139], v[226:229], v[88:91]
	v_mfma_f32_16x16x32_bf16 v[84:87], v[144:147], v[226:229], v[84:87]
	v_mfma_f32_16x16x32_bf16 v[72:75], v[136:139], v[234:237], v[72:75]
	v_mfma_f32_16x16x32_bf16 v[68:71], v[144:147], v[234:237], v[68:71]
	v_mfma_f32_16x16x32_bf16 v[128:131], v[148:151], v[190:193], v[128:131]
	v_mfma_f32_16x16x32_bf16 v[124:127], v[178:181], v[190:193], v[124:127]
	v_mfma_f32_16x16x32_bf16 v[112:115], v[148:151], v[198:201], v[112:115]
	v_mfma_f32_16x16x32_bf16 v[108:111], v[178:181], v[198:201], v[108:111]
	v_mfma_f32_16x16x32_bf16 v[96:99], v[148:151], v[222:225], v[96:99]
	v_mfma_f32_16x16x32_bf16 v[92:95], v[178:181], v[222:225], v[92:95]
	v_mfma_f32_16x16x32_bf16 v[80:83], v[148:151], v[230:233], v[80:83]
	v_mfma_f32_16x16x32_bf16 v[76:79], v[178:181], v[230:233], v[76:79]
	v_mfma_f32_16x16x32_bf16 v[128:131], v[152:155], v[194:197], v[128:131]
	v_mfma_f32_16x16x32_bf16 v[124:127], v[186:189], v[194:197], v[124:127]
	v_mfma_f32_16x16x32_bf16 v[112:115], v[152:155], v[202:205], v[112:115]
	v_mfma_f32_16x16x32_bf16 v[108:111], v[186:189], v[202:205], v[108:111]
	v_mfma_f32_16x16x32_bf16 v[96:99], v[152:155], v[226:229], v[96:99]
	v_mfma_f32_16x16x32_bf16 v[92:95], v[186:189], v[226:229], v[92:95]
	v_mfma_f32_16x16x32_bf16 v[80:83], v[152:155], v[234:237], v[80:83]
	v_mfma_f32_16x16x32_bf16 v[76:79], v[186:189], v[234:237], v[76:79]
	s_barrier
	s_setprio 0
	s_add_i32 s28, s28, s1
	v_lshl_add_u64 v[182:183], s[24:25], 0, v[2:3]
	s_mov_b32 m0, s28
	ds_read_b128 v[190:193], v184 offset:16384
	ds_read_b128 v[194:197], v184 offset:17408
	ds_read_b128 v[198:201], v184 offset:18432
	ds_read_b128 v[202:205], v184 offset:19456
	ds_read_b128 v[222:225], v184 offset:20480
	ds_read_b128 v[226:229], v184 offset:21504
	ds_read_b128 v[230:233], v184 offset:22528
	ds_read_b128 v[234:237], v184 offset:23552
	global_load_lds_dwordx4 v[182:183], off
	s_add_i32 m0, s28, 0x2000
	s_add_u32 s28, s24, 0x100000
	v_lshl_add_u64 v[238:239], s[24:25], 0, v[168:169]
	s_addc_u32 s29, s25, 0
	s_add_i32 s71, s71, s1
	global_load_lds_dwordx4 v[238:239], off
	v_lshl_add_u64 v[240:241], s[28:29], 0, v[2:3]
	s_mov_b32 m0, s71
	v_lshl_add_u64 v[242:243], s[26:27], 0, v[170:171]
	global_load_lds_dwordx4 v[240:241], off
	v_lshl_add_u64 v[240:241], s[28:29], 0, v[168:169]
	s_add_i32 m0, s71, 0x2000
	s_nop 0
	global_load_lds_dwordx4 v[240:241], off
	v_lshl_add_u64 v[240:241], s[26:27], 0, v[172:173]
	s_mov_b32 m0, s46
	s_nop 0
	global_load_lds_dwordx4 v[240:241], off
	s_mov_b32 m0, s50
	s_nop 0
	global_load_lds_dwordx4 v[242:243], off
	s_waitcnt vmcnt(8)
	s_waitcnt lgkmcnt(0)
	s_setprio 1
	s_barrier
	v_mfma_f32_16x16x32_bf16 v[56:59], v[132:135], v[190:193], v[56:59]
	v_mfma_f32_16x16x32_bf16 v[52:55], v[140:143], v[190:193], v[52:55]
	v_mfma_f32_16x16x32_bf16 v[40:43], v[132:135], v[198:201], v[40:43]
	v_mfma_f32_16x16x32_bf16 v[36:39], v[140:143], v[198:201], v[36:39]
	v_mfma_f32_16x16x32_bf16 v[24:27], v[132:135], v[222:225], v[24:27]
	v_mfma_f32_16x16x32_bf16 v[20:23], v[140:143], v[222:225], v[20:23]
	v_mfma_f32_16x16x32_bf16 v[8:11], v[132:135], v[230:233], v[8:11]
	v_mfma_f32_16x16x32_bf16 v[4:7], v[140:143], v[230:233], v[4:7]
	v_mfma_f32_16x16x32_bf16 v[56:59], v[136:139], v[194:197], v[56:59]
	v_mfma_f32_16x16x32_bf16 v[52:55], v[144:147], v[194:197], v[52:55]
	v_mfma_f32_16x16x32_bf16 v[40:43], v[136:139], v[202:205], v[40:43]
	v_mfma_f32_16x16x32_bf16 v[36:39], v[144:147], v[202:205], v[36:39]
	v_mfma_f32_16x16x32_bf16 v[24:27], v[136:139], v[226:229], v[24:27]
	v_mfma_f32_16x16x32_bf16 v[20:23], v[144:147], v[226:229], v[20:23]
	v_mfma_f32_16x16x32_bf16 v[8:11], v[136:139], v[234:237], v[8:11]
	v_mfma_f32_16x16x32_bf16 v[4:7], v[144:147], v[234:237], v[4:7]
	v_mfma_f32_16x16x32_bf16 v[64:67], v[148:151], v[190:193], v[64:67]
	v_mfma_f32_16x16x32_bf16 v[60:63], v[178:181], v[190:193], v[60:63]
	v_mfma_f32_16x16x32_bf16 v[48:51], v[148:151], v[198:201], v[48:51]
	v_mfma_f32_16x16x32_bf16 v[44:47], v[178:181], v[198:201], v[44:47]
	v_mfma_f32_16x16x32_bf16 v[32:35], v[148:151], v[222:225], v[32:35]
	v_mfma_f32_16x16x32_bf16 v[28:31], v[178:181], v[222:225], v[28:31]
	v_mfma_f32_16x16x32_bf16 v[16:19], v[148:151], v[230:233], v[16:19]
	v_mfma_f32_16x16x32_bf16 v[12:15], v[178:181], v[230:233], v[12:15]
	v_mfma_f32_16x16x32_bf16 v[64:67], v[152:155], v[194:197], v[64:67]
	v_mfma_f32_16x16x32_bf16 v[60:63], v[186:189], v[194:197], v[60:63]
	v_mfma_f32_16x16x32_bf16 v[48:51], v[152:155], v[202:205], v[48:51]
	v_mfma_f32_16x16x32_bf16 v[44:47], v[186:189], v[202:205], v[44:47]
	v_mfma_f32_16x16x32_bf16 v[32:35], v[152:155], v[226:229], v[32:35]
	v_mfma_f32_16x16x32_bf16 v[28:31], v[186:189], v[226:229], v[28:31]
	v_mfma_f32_16x16x32_bf16 v[16:19], v[152:155], v[234:237], v[16:19]
	v_mfma_f32_16x16x32_bf16 v[12:15], v[186:189], v[234:237], v[12:15]
	s_barrier
	s_setprio 0
	s_add_i32 s28, 0, 0x18000
	s_add_i32 s29, 0, 0x1c000
	v_add_u32_e32 v144, s28, v163
	v_add_u32_e32 v185, s29, v163
	ds_read_b128 v[132:135], v144
	ds_read_b128 v[136:139], v144 offset:1024
	ds_read_b128 v[140:143], v144 offset:2048
	ds_read_b128 v[144:147], v144 offset:3072
	ds_read_b128 v[148:151], v185
	ds_read_b128 v[152:155], v185 offset:1024
	ds_read_b128 v[178:181], v185 offset:2048
	ds_read_b128 v[186:189], v185 offset:3072
	s_add_u32 s26, s26, 0x100000
	s_addc_u32 s27, s27, 0
	s_mov_b32 m0, s51
	v_lshl_add_u64 v[244:245], s[26:27], 0, v[172:173]
	ds_read_b128 v[190:193], v184 offset:32768
	ds_read_b128 v[194:197], v184 offset:33792
	ds_read_b128 v[198:201], v184 offset:34816
	ds_read_b128 v[202:205], v184 offset:35840
	ds_read_b128 v[222:225], v184 offset:36864
	ds_read_b128 v[226:229], v184 offset:37888
	ds_read_b128 v[230:233], v184 offset:38912
	ds_read_b128 v[234:237], v184 offset:39936
	global_load_lds_dwordx4 v[244:245], off
	v_lshl_add_u64 v[244:245], s[26:27], 0, v[170:171]
	s_mov_b32 m0, s54
	s_nop 0
	global_load_lds_dwordx4 v[244:245], off
	s_waitcnt vmcnt(8)
	s_waitcnt lgkmcnt(0)
	s_setprio 1
	s_barrier
	v_mfma_f32_16x16x32_bf16 v[120:123], v[132:135], v[190:193], v[120:123]
	v_mfma_f32_16x16x32_bf16 v[116:119], v[140:143], v[190:193], v[116:119]
	v_mfma_f32_16x16x32_bf16 v[104:107], v[132:135], v[198:201], v[104:107]
	v_mfma_f32_16x16x32_bf16 v[100:103], v[140:143], v[198:201], v[100:103]
	v_mfma_f32_16x16x32_bf16 v[88:91], v[132:135], v[222:225], v[88:91]
	v_mfma_f32_16x16x32_bf16 v[84:87], v[140:143], v[222:225], v[84:87]
	v_mfma_f32_16x16x32_bf16 v[72:75], v[132:135], v[230:233], v[72:75]
	v_mfma_f32_16x16x32_bf16 v[68:71], v[140:143], v[230:233], v[68:71]
	v_mfma_f32_16x16x32_bf16 v[120:123], v[136:139], v[194:197], v[120:123]
	v_mfma_f32_16x16x32_bf16 v[116:119], v[144:147], v[194:197], v[116:119]
	v_mfma_f32_16x16x32_bf16 v[104:107], v[136:139], v[202:205], v[104:107]
	v_mfma_f32_16x16x32_bf16 v[100:103], v[144:147], v[202:205], v[100:103]
	v_mfma_f32_16x16x32_bf16 v[88:91], v[136:139], v[226:229], v[88:91]
	v_mfma_f32_16x16x32_bf16 v[84:87], v[144:147], v[226:229], v[84:87]
	v_mfma_f32_16x16x32_bf16 v[72:75], v[136:139], v[234:237], v[72:75]
	v_mfma_f32_16x16x32_bf16 v[68:71], v[144:147], v[234:237], v[68:71]
	v_mfma_f32_16x16x32_bf16 v[128:131], v[148:151], v[190:193], v[128:131]
	v_mfma_f32_16x16x32_bf16 v[124:127], v[178:181], v[190:193], v[124:127]
	v_mfma_f32_16x16x32_bf16 v[112:115], v[148:151], v[198:201], v[112:115]
	v_mfma_f32_16x16x32_bf16 v[108:111], v[178:181], v[198:201], v[108:111]
	v_mfma_f32_16x16x32_bf16 v[96:99], v[148:151], v[222:225], v[96:99]
	v_mfma_f32_16x16x32_bf16 v[92:95], v[178:181], v[222:225], v[92:95]
	v_mfma_f32_16x16x32_bf16 v[80:83], v[148:151], v[230:233], v[80:83]
	v_mfma_f32_16x16x32_bf16 v[76:79], v[178:181], v[230:233], v[76:79]
	v_mfma_f32_16x16x32_bf16 v[128:131], v[152:155], v[194:197], v[128:131]
	v_mfma_f32_16x16x32_bf16 v[124:127], v[186:189], v[194:197], v[124:127]
	v_mfma_f32_16x16x32_bf16 v[112:115], v[152:155], v[202:205], v[112:115]
	v_mfma_f32_16x16x32_bf16 v[108:111], v[186:189], v[202:205], v[108:111]
	v_mfma_f32_16x16x32_bf16 v[96:99], v[152:155], v[226:229], v[96:99]
	v_mfma_f32_16x16x32_bf16 v[92:95], v[186:189], v[226:229], v[92:95]
	v_mfma_f32_16x16x32_bf16 v[80:83], v[152:155], v[234:237], v[80:83]
	v_mfma_f32_16x16x32_bf16 v[76:79], v[186:189], v[234:237], v[76:79]
	s_barrier
	s_setprio 0
	s_add_i32 s26, s28, s1
	v_lshl_add_u64 v[182:183], v[182:183], 0, s[86:87]
	s_mov_b32 m0, s26
	ds_read_b128 v[190:193], v184 offset:49152
	ds_read_b128 v[194:197], v184 offset:50176
	ds_read_b128 v[198:201], v184 offset:51200
	ds_read_b128 v[202:205], v184 offset:52224
	ds_read_b128 v[222:225], v184 offset:53248
	ds_read_b128 v[226:229], v184 offset:54272
	ds_read_b128 v[230:233], v184 offset:55296
	ds_read_b128 v[234:237], v184 offset:56320
	global_load_lds_dwordx4 v[182:183], off
	s_add_i32 m0, s26, 0x2000
	s_add_u32 s24, s24, 0x100080
	v_lshl_add_u64 v[182:183], v[238:239], 0, s[86:87]
	s_addc_u32 s25, s25, 0
	s_add_i32 s26, s29, s1
	global_load_lds_dwordx4 v[182:183], off
	v_lshl_add_u64 v[182:183], s[24:25], 0, v[2:3]
	s_mov_b32 m0, s26
	s_nop 0
	global_load_lds_dwordx4 v[182:183], off
	v_lshl_add_u64 v[182:183], s[24:25], 0, v[168:169]
	s_add_i32 m0, s26, 0x2000
	s_nop 0
	global_load_lds_dwordx4 v[182:183], off
	v_lshl_add_u64 v[182:183], v[240:241], 0, s[86:87]
	s_mov_b32 m0, s78
	s_nop 0
	global_load_lds_dwordx4 v[182:183], off
	v_lshl_add_u64 v[182:183], v[242:243], 0, s[86:87]
	s_mov_b32 m0, s85
	s_nop 0
	global_load_lds_dwordx4 v[182:183], off
	s_waitcnt vmcnt(8)
	s_waitcnt lgkmcnt(0)
	s_setprio 1
	s_barrier
	v_mfma_f32_16x16x32_bf16 v[56:59], v[132:135], v[190:193], v[56:59]
	v_mfma_f32_16x16x32_bf16 v[52:55], v[140:143], v[190:193], v[52:55]
	v_mfma_f32_16x16x32_bf16 v[40:43], v[132:135], v[198:201], v[40:43]
	v_mfma_f32_16x16x32_bf16 v[36:39], v[140:143], v[198:201], v[36:39]
	v_mfma_f32_16x16x32_bf16 v[24:27], v[132:135], v[222:225], v[24:27]
	v_mfma_f32_16x16x32_bf16 v[20:23], v[140:143], v[222:225], v[20:23]
	v_mfma_f32_16x16x32_bf16 v[8:11], v[132:135], v[230:233], v[8:11]
	v_mfma_f32_16x16x32_bf16 v[4:7], v[140:143], v[230:233], v[4:7]
	v_mfma_f32_16x16x32_bf16 v[56:59], v[136:139], v[194:197], v[56:59]
	v_mfma_f32_16x16x32_bf16 v[52:55], v[144:147], v[194:197], v[52:55]
	v_mfma_f32_16x16x32_bf16 v[40:43], v[136:139], v[202:205], v[40:43]
	v_mfma_f32_16x16x32_bf16 v[36:39], v[144:147], v[202:205], v[36:39]
	v_mfma_f32_16x16x32_bf16 v[24:27], v[136:139], v[226:229], v[24:27]
	v_mfma_f32_16x16x32_bf16 v[20:23], v[144:147], v[226:229], v[20:23]
	v_mfma_f32_16x16x32_bf16 v[8:11], v[136:139], v[234:237], v[8:11]
	v_mfma_f32_16x16x32_bf16 v[4:7], v[144:147], v[234:237], v[4:7]
	v_mfma_f32_16x16x32_bf16 v[64:67], v[148:151], v[190:193], v[64:67]
	v_mfma_f32_16x16x32_bf16 v[60:63], v[178:181], v[190:193], v[60:63]
	v_mfma_f32_16x16x32_bf16 v[48:51], v[148:151], v[198:201], v[48:51]
	v_mfma_f32_16x16x32_bf16 v[44:47], v[178:181], v[198:201], v[44:47]
	v_mfma_f32_16x16x32_bf16 v[32:35], v[148:151], v[222:225], v[32:35]
	v_mfma_f32_16x16x32_bf16 v[28:31], v[178:181], v[222:225], v[28:31]
	v_mfma_f32_16x16x32_bf16 v[16:19], v[148:151], v[230:233], v[16:19]
	v_mfma_f32_16x16x32_bf16 v[12:15], v[178:181], v[230:233], v[12:15]
	v_mfma_f32_16x16x32_bf16 v[64:67], v[152:155], v[194:197], v[64:67]
	v_mfma_f32_16x16x32_bf16 v[60:63], v[186:189], v[194:197], v[60:63]
	v_mfma_f32_16x16x32_bf16 v[48:51], v[152:155], v[202:205], v[48:51]
	v_mfma_f32_16x16x32_bf16 v[44:47], v[186:189], v[202:205], v[44:47]
	v_mfma_f32_16x16x32_bf16 v[32:35], v[152:155], v[226:229], v[32:35]
	v_mfma_f32_16x16x32_bf16 v[28:31], v[186:189], v[226:229], v[28:31]
	v_mfma_f32_16x16x32_bf16 v[16:19], v[152:155], v[234:237], v[16:19]
	v_mfma_f32_16x16x32_bf16 v[12:15], v[186:189], v[234:237], v[12:15]
	s_barrier
	s_setprio 0
	s_add_i32 s58, s58, 2
	s_add_u32 s6, s6, 0x100
	s_addc_u32 s7, s7, 0
	s_add_u32 s21, s21, 0x100
	s_addc_u32 s13, s13, 0
	s_cmp_gt_u32 s58, 61
	s_cbranch_scc0 .LBB0_265
	s_nop 0
	s_and_b64 vcc, exec, s[30:31]
	s_cbranch_vccz .LBB0_268
	s_barrier
